# speedup vs baseline: 1.0812x; 1.0170x over previous
_Z9bn_kernelPKDF16_PKfS2_S2_S2_Pfi:
	s_load_dword s8, s[0:1], 0x30
	s_load_dwordx4 s[4:7], s[0:1], 0x0
	s_load_dwordx4 s[12:15], s[0:1], 0x10
	s_load_dwordx2 s[16:17], s[0:1], 0x20
	s_load_dwordx2 s[18:19], s[0:1], 0x28
	s_load_dword s20, s[0:1], 0x38
	s_lshl_b32 s10, s2, 6
	v_lshrrev_b32_e32 v1, 4, v0
	v_or_b32_e32 v34, s10, v1
	s_waitcnt lgkmcnt(0)
	s_add_i32 s9, s8, -1
	v_min_i32_e32 v6, s9, v34
	v_or_b32_e32 v3, 16, v34
	v_lshlrev_b32_e32 v2, 2, v0
	v_ashrrev_i32_e32 v7, 31, v6
	v_min_i32_e32 v8, s9, v3
	v_and_b32_e32 v4, 60, v2
	v_lshlrev_b64 v[6:7], 8, v[6:7]
	v_ashrrev_i32_e32 v9, 31, v8
	v_mov_b32_e32 v37, 0
	v_lshl_add_u64 v[6:7], s[4:5], 0, v[6:7]
	v_lshlrev_b32_e32 v36, 1, v4
	v_lshlrev_b64 v[8:9], 8, v[8:9]
	v_lshl_add_u64 v[6:7], v[6:7], 0, v[36:37]
	v_lshl_add_u64 v[8:9], s[4:5], 0, v[8:9]
	v_or_b32_e32 v3, 32, v34
	v_lshl_add_u64 v[8:9], v[8:9], 0, v[36:37]
	v_and_b32_e32 v63, 0x1fc, v2
	global_load_dword v64, v63, s[12:13]
	global_load_dword v65, v63, s[14:15]
	global_load_dword v63, v63, s[16:17]
	global_load_dwordx2 v[22:23], v[6:7], off
	global_load_dwordx2 v[24:25], v[6:7], off offset:128
	global_load_dwordx2 v[18:19], v[8:9], off
	global_load_dwordx2 v[20:21], v[8:9], off offset:128
	v_min_i32_e32 v6, s9, v3
	v_or_b32_e32 v3, 48, v34
	v_min_i32_e32 v8, s9, v3
	v_mov_b32_e32 v3, v37
	v_lshl_add_u64 v[10:11], s[6:7], 0, v[2:3]
	global_load_dword v3, v2, s[6:7]
	global_load_dword v5, v2, s[6:7] offset:1024
	global_load_dword v35, v2, s[6:7] offset:2048
	s_movk_i32 s2, 0x1000
	v_add_co_u32_e32 v12, vcc, s2, v10
	s_movk_i32 s2, 0x2000
	s_nop 0
	v_addc_co_u32_e32 v13, vcc, 0, v11, vcc
	v_add_co_u32_e32 v14, vcc, s2, v10
	s_movk_i32 s2, 0x3000
	s_nop 0
	v_addc_co_u32_e32 v15, vcc, 0, v11, vcc
	global_load_dword v38, v[12:13], off offset:1024
	global_load_dword v39, v[12:13], off offset:2048
	global_load_dword v40, v[12:13], off offset:3072
	v_add_co_u32_e32 v12, vcc, s2, v10
	s_movk_i32 s2, 0x4000
	s_nop 0
	v_addc_co_u32_e32 v13, vcc, 0, v11, vcc
	v_add_co_u32_e32 v16, vcc, s2, v10
	s_movk_i32 s2, 0x5000
	s_nop 0
	v_addc_co_u32_e32 v17, vcc, 0, v11, vcc
	global_load_dword v41, v2, s[6:7] offset:3072
	global_load_dword v42, v[14:15], off offset:-4096
	global_load_dword v43, v[14:15], off
	global_load_dword v44, v[14:15], off offset:1024
	global_load_dword v45, v[14:15], off offset:2048
	global_load_dword v46, v[14:15], off offset:3072
	global_load_dword v47, v[16:17], off offset:-4096
	global_load_dword v48, v[16:17], off
	v_add_co_u32_e32 v14, vcc, s2, v10
	s_movk_i32 s2, 0x6000
	s_nop 0
	v_addc_co_u32_e32 v15, vcc, 0, v11, vcc
	v_add_co_u32_e32 v26, vcc, s2, v10
	v_ashrrev_i32_e32 v7, 31, v6
	s_nop 0
	v_addc_co_u32_e32 v27, vcc, 0, v11, vcc
	global_load_dword v49, v[12:13], off offset:1024
	global_load_dword v50, v[12:13], off offset:2048
	global_load_dword v51, v[12:13], off offset:3072
	global_load_dword v52, v[14:15], off offset:1024
	global_load_dword v53, v[14:15], off offset:2048
	global_load_dword v54, v[14:15], off offset:3072
	global_load_dword v55, v[16:17], off offset:1024
	global_load_dword v56, v[16:17], off offset:2048
	global_load_dword v57, v[16:17], off offset:3072
	global_load_dword v58, v[26:27], off offset:-4096
	global_load_dword v59, v[26:27], off
	global_load_dword v60, v[26:27], off offset:1024
	global_load_dword v61, v[26:27], off offset:2048
	global_load_dword v62, v[26:27], off offset:3072
	v_lshlrev_b64 v[6:7], 8, v[6:7]
	v_ashrrev_i32_e32 v9, 31, v8
	s_movk_i32 s2, 0x7000
	v_lshl_add_u64 v[6:7], s[4:5], 0, v[6:7]
	v_add_co_u32_e32 v10, vcc, s2, v10
	v_lshlrev_b64 v[8:9], 8, v[8:9]
	v_lshl_add_u64 v[6:7], v[6:7], 0, v[36:37]
	v_addc_co_u32_e32 v11, vcc, 0, v11, vcc
	v_lshl_add_u64 v[8:9], s[4:5], 0, v[8:9]
	global_load_dword v12, v[10:11], off
	global_load_dword v13, v[10:11], off offset:1024
	global_load_dword v14, v[10:11], off offset:2048
	global_load_dword v15, v[10:11], off offset:3072
	v_lshl_add_u64 v[8:9], v[8:9], 0, v[36:37]
	global_load_dwordx2 v[30:31], v[6:7], off
	global_load_dwordx2 v[32:33], v[6:7], off offset:128
	global_load_dwordx2 v[26:27], v[8:9], off
	global_load_dwordx2 v[28:29], v[8:9], off offset:128
	s_movk_i32 s2, 0x80
	v_cmp_gt_u32_e32 vcc, s2, v0
	s_waitcnt vmcnt(35)
	v_add_f32_e32 v3, 0, v3
	s_waitcnt vmcnt(34)
	v_add_f32_e32 v3, v3, v5
	s_waitcnt vmcnt(33)
	v_add_f32_e32 v3, v3, v35
	s_waitcnt vmcnt(29)
	v_add_f32_e32 v3, v3, v41
	s_waitcnt vmcnt(28)
	v_add_f32_e32 v3, v3, v42
	v_add_f32_e32 v3, v3, v38
	v_add_f32_e32 v3, v3, v39
	v_add_f32_e32 v3, v3, v40
	s_waitcnt vmcnt(27)
	v_add_f32_e32 v3, v3, v43
	s_waitcnt vmcnt(26)
	v_add_f32_e32 v3, v3, v44
	s_waitcnt vmcnt(25)
	v_add_f32_e32 v3, v3, v45
	s_waitcnt vmcnt(24)
	v_add_f32_e32 v3, v3, v46
	s_waitcnt vmcnt(23)
	v_add_f32_e32 v3, v3, v47
	s_waitcnt vmcnt(21)
	v_add_f32_e32 v3, v3, v49
	s_waitcnt vmcnt(20)
	v_add_f32_e32 v3, v3, v50
	s_waitcnt vmcnt(19)
	v_add_f32_e32 v3, v3, v51
	v_add_f32_e32 v3, v3, v48
	s_waitcnt vmcnt(15)
	v_add_f32_e32 v3, v3, v55
	s_waitcnt vmcnt(14)
	v_add_f32_e32 v3, v3, v56
	s_waitcnt vmcnt(13)
	v_add_f32_e32 v3, v3, v57
	s_waitcnt vmcnt(12)
	v_add_f32_e32 v3, v3, v58
	v_add_f32_e32 v3, v3, v52
	v_add_f32_e32 v3, v3, v53
	v_add_f32_e32 v3, v3, v54
	s_waitcnt vmcnt(11)
	v_add_f32_e32 v3, v3, v59
	s_waitcnt vmcnt(10)
	v_add_f32_e32 v3, v3, v60
	s_waitcnt vmcnt(9)
	v_add_f32_e32 v3, v3, v61
	s_waitcnt vmcnt(8)
	v_add_f32_e32 v3, v3, v62
	s_waitcnt vmcnt(7)
	v_add_f32_e32 v3, v3, v12
	s_waitcnt vmcnt(6)
	v_add_f32_e32 v3, v3, v13
	s_waitcnt vmcnt(5)
	v_add_f32_e32 v3, v3, v14
	s_waitcnt vmcnt(4)
	v_add_f32_e32 v3, v3, v15
	ds_write_b32 v2, v3
	s_waitcnt lgkmcnt(0)
	s_barrier
	s_and_saveexec_b64 s[2:3], vcc
	s_cbranch_execz .LBB3_2
	v_cvt_f32_i32_e32 v8, s8
	s_mov_b32 s11, 0x800000
	v_mov_b32_e32 v3, v64
	v_mov_b32_e32 v5, v65
	v_div_scale_f32 v10, s[6:7], v8, v8, 1.0
	v_rcp_f32_e32 v11, v10
	ds_read2st64_b32 v[14:15], v2 offset1:2
	v_div_scale_f32 v12, vcc, 1.0, v8, 1.0
	v_fma_f32 v13, -v10, v11, 1.0
	v_fmac_f32_e32 v11, v13, v11
	v_mul_f32_e32 v13, v12, v11
	s_waitcnt lgkmcnt(0)
	v_mov_b32_e32 v7, v14
	v_fma_f32 v14, -v10, v13, v12
	v_fmac_f32_e32 v13, v14, v11
	v_fma_f32 v10, -v10, v13, v12
	v_div_fmas_f32 v10, v10, v11, v13
	v_mov_b32_e32 v6, v15
	v_div_fixup_f32 v8, v10, v8, 1.0
	v_mov_b32_e32 v9, v63
	v_pk_mul_f32 v[6:7], v[8:9], v[6:7] op_sel_hi:[0,1]
	v_fma_f32 v6, -v7, v7, v6
	v_max_f32_e32 v6, 0, v6
	v_add_f32_e32 v6, 0x3727c5ac, v6
	v_mul_f32_e32 v8, 0x4b800000, v6
	v_cmp_gt_f32_e32 vcc, s11, v6
	v_add_f32_e32 v7, v7, v3
	v_sub_f32_e32 v3, v3, v7
	v_cndmask_b32_e32 v6, v6, v8, vcc
	v_rsq_f32_e32 v6, v6
	s_nop 0
	v_mul_f32_e32 v8, 0x45800000, v6
	v_cndmask_b32_e32 v6, v6, v8, vcc
	v_mul_f32_e32 v5, v5, v6
	v_fmac_f32_e32 v9, v3, v5
	ds_write2st64_b32 v2, v5, v9 offset0:4 offset1:6

.LBB3_5:
	v_add_u32_e32 v34, s0, v40
	v_subrev_u32_e32 v35, 48, v34
	v_min_i32_e32 v42, s9, v35
	v_ashrrev_i32_e32 v43, 31, v42
	v_lshlrev_b64 v[42:43], 8, v[42:43]
	v_subrev_u32_e32 v41, 32, v34
	v_lshl_add_u64 v[50:51], v[38:39], 0, v[42:43]
	v_min_i32_e32 v42, s9, v41
	v_ashrrev_i32_e32 v43, 31, v42
	v_lshlrev_b64 v[42:43], 8, v[42:43]
	v_add_u32_e32 v41, -16, v34
	v_lshl_add_u64 v[52:53], v[38:39], 0, v[42:43]
	global_load_dwordx2 v[46:47], v[50:51], off
	global_load_dwordx2 v[42:43], v[50:51], off offset:128
	global_load_dwordx2 v[48:49], v[52:53], off
	global_load_dwordx2 v[44:45], v[52:53], off offset:128
	v_min_i32_e32 v50, s9, v41
	v_ashrrev_i32_e32 v51, 31, v50
	v_lshlrev_b64 v[50:51], 8, v[50:51]
	v_lshl_add_u64 v[58:59], v[38:39], 0, v[50:51]
	v_min_i32_e32 v50, s9, v34
	v_ashrrev_i32_e32 v51, 31, v50
	v_lshlrev_b64 v[50:51], 8, v[50:51]
	v_lshl_add_u64 v[60:61], v[38:39], 0, v[50:51]
	global_load_dwordx2 v[54:55], v[58:59], off
	global_load_dwordx2 v[50:51], v[58:59], off offset:128
	global_load_dwordx2 v[56:57], v[60:61], off
	global_load_dwordx2 v[52:53], v[60:61], off offset:128
	v_fma_mix_f32 v41, v2, v22, v10 op_sel_hi:[0,1,0]
	v_fma_mix_f32 v22, v3, v22, v11 op_sel:[0,1,0] op_sel_hi:[0,1,0]
	v_max_f32_e32 v59, 0, v22
	v_fma_mix_f32 v22, v7, v24, v15 op_sel:[0,1,0] op_sel_hi:[0,1,0]
	v_max_f32_e32 v63, 0, v22
	v_fma_mix_f32 v22, v4, v23, v12 op_sel_hi:[0,1,0]
	v_max_f32_e32 v60, 0, v22
	v_fma_mix_f32 v22, v8, v25, v16 op_sel_hi:[0,1,0]
	v_max_f32_e32 v64, 0, v22
	v_fma_mix_f32 v22, v5, v23, v13 op_sel:[0,1,0] op_sel_hi:[0,1,0]
	v_max_f32_e32 v61, 0, v22
	v_fma_mix_f32 v22, v9, v25, v17 op_sel:[0,1,0] op_sel_hi:[0,1,0]
	v_max_f32_e32 v65, 0, v22
	v_subrev_u32_e32 v22, 32, v40
	v_max_f32_e32 v58, 0, v41
	v_fma_mix_f32 v41, v6, v24, v14 op_sel_hi:[0,1,0]
	v_cmp_gt_i32_e32 vcc, s8, v22
	v_max_f32_e32 v62, 0, v41
	global_store_dwordx4 v[0:1], v[58:61], off offset:-256
	global_store_dwordx4 v[0:1], v[62:65], off
	s_and_saveexec_b64 s[6:7], vcc
	s_cbranch_execz .LBB3_7
	v_fma_mix_f32 v23, v2, v18, v10 op_sel_hi:[0,1,0]
	v_fma_mix_f32 v18, v3, v18, v11 op_sel:[0,1,0] op_sel_hi:[0,1,0]
	v_max_f32_e32 v59, 0, v18
	v_fma_mix_f32 v18, v7, v20, v15 op_sel:[0,1,0] op_sel_hi:[0,1,0]
	v_max_f32_e32 v63, 0, v18
	v_fma_mix_f32 v18, v4, v19, v12 op_sel_hi:[0,1,0]
	v_max_f32_e32 v60, 0, v18
	v_fma_mix_f32 v18, v8, v21, v16 op_sel_hi:[0,1,0]
	v_max_f32_e32 v58, 0, v23
	v_fma_mix_f32 v23, v6, v20, v14 op_sel_hi:[0,1,0]
	v_max_f32_e32 v64, 0, v18
	v_fma_mix_f32 v18, v5, v19, v13 op_sel:[0,1,0] op_sel_hi:[0,1,0]
	v_max_f32_e32 v62, 0, v23
	v_max_f32_e32 v61, 0, v18
	v_fma_mix_f32 v18, v9, v21, v17 op_sel:[0,1,0] op_sel_hi:[0,1,0]
	v_ashrrev_i32_e32 v23, 31, v22
	v_max_f32_e32 v65, 0, v18
	v_lshlrev_b64 v[18:19], 9, v[22:23]
	v_lshl_add_u64 v[18:19], v[36:37], 0, v[18:19]
	global_store_dwordx4 v[18:19], v[58:61], off
	global_store_dwordx4 v[18:19], v[62:65], off offset:256
